# rotation: all 8 experts' fp6 gate/up conversion hosted in attention, MoE-down e4m3 conversion moved to the MoE gate/up GEMM epilogues, no fp6 conversion left in P0 (on the P18 count-reduction base)
# speedup vs baseline: 1.0097x; 1.0021x over previous
; template <int MODE>
; __device__ __forceinline__ void tr_matrix6(const float* W, int nb, int K, int N, unsigned char* WT, int drows, int rot, int gw, int NGW, int lane, float wscale) {
;     const int nbn = N / 32, per = (K / 256) * nbn, total = nb * per;
;     int it = gw - rot; if (it < 0) it += NGW;
;     const int c = lane & 7, q = lane >> 3;
;     for (; it < total; it += NGW) {
;         const int e = it / per, r = it - e * per, kb = r / nbn, nbk = r - kb * nbn, n0 = nbk * 32, k0 = kb * 256;
;         const float* src = W + (size_t)e * K * N + (size_t)(k0 + 32 * q) * N + n0 + 4 * c;
.LBB0_54:
	s_add_u32 s40, s70, 0x8a00000
	s_addc_u32 s41, s71, 0
	v_readlane_b32 s6, v251, 9
	s_cmpk_lt_i32 s6, 0x7d0
	s_cselect_b32 s0, s72, 0
	s_add_i32 s0, s6, s0
	s_add_i32 s3, s0, 0xfffff830
	s_cmpk_gt_i32 s3, 0xffff
	v_readlane_b32 s7, v251, 10
	s_cbranch_scc1 .LBB0_59
	v_readlane_b32 s48, v251, 29
	v_readlane_b32 s60, v251, 41
	v_readlane_b32 s61, v251, 42
	v_and_b32_e32 v132, 28, v144
	v_mov_b32_e32 v130, 0
	v_readlane_b32 s62, v251, 43
	v_readlane_b32 s63, v251, 44
	s_mov_b64 s[20:21], s[60:61]
	v_and_b32_e32 v146, 0xe0, v144
	v_mov_b32_e32 v147, v130
	s_movk_i32 s0, 0x7000
	v_lshlrev_b32_e32 v148, 2, v132
	v_mov_b32_e32 v149, v130
	s_mov_b32 s1, 0x93000
	s_mov_b32 s5, 0x9a000
	s_mov_b32 s14, 0xa1000
	s_mov_b32 s15, 0xa8000
	s_mov_b32 s16, 0xaf000
	s_mov_b32 s17, 0xb6000
	s_mov_b32 s33, 0xbd000
	s_mov_b32 s38, 0xc4000
	s_mov_b32 s39, 0xcb000
	s_mov_b32 s42, 0xd2000
	s_mov_b32 s43, 0xd9000
	s_mov_b32 s44, 0xc0f00000
	v_mov_b32_e32 v133, 0x40f00000
	s_movk_i32 s45, 0x1000
	s_mov_b32 s46, s3
	s_mov_b64 s[22:23], s[62:63]
	v_readlane_b32 s49, v251, 30
	v_readlane_b32 s50, v251, 31
	v_readlane_b32 s51, v251, 32
	v_readlane_b32 s52, v251, 33
	v_readlane_b32 s53, v251, 34
	v_readlane_b32 s54, v251, 35
	v_readlane_b32 s55, v251, 36
	v_readlane_b32 s56, v251, 37
	v_readlane_b32 s57, v251, 38
	v_readlane_b32 s58, v251, 39
	v_readlane_b32 s59, v251, 40

; #define RP(n) _Pragma("nounroll") for (int rep_ = 0; rep_ < (int)(((REPEAT) >> (n)) & 1u) + 1; ++rep_)
; __global__ void __launch_bounds__(NTHREADS, 2) fwd_kernel(Args args) {
;     ...
;     if (PH(15)) RP(15)
;     {
;         const int vcu = (G % 8 == 0) ? (bx % 8) * (G / 8) + bx / 8 : bx;
;         att::CvtState cs{args.in[I_MOED], ws + W_MOED, gw * att::CV_IPW, (gw + 1) * att::CV_IPW};
;         for (int L = vcu; L < NBATCH * NH * 8; L += G) {
.LBB0_1020:
	s_or_b64 exec, exec, s[4:5]
	s_lshr_b32 s0, s3, 29
	s_add_i32 s5, s2, s0
	s_and_b32 s0, s5, -8
	s_ashr_i32 s1, s76, 3
	s_sub_i32 s0, s2, s0
	s_mul_i32 s8, s1, s0
	s_ashr_i32 s1, s5, 3
	s_and_b32 s4, s76, 7
	s_add_i32 s5, s8, s1
	v_readlane_b32 s8, v251, 9
	s_add_u32 s30, s70, 0x24a00000
	s_mul_i32 s35, s8, 28
	s_addc_u32 s31, s71, 0
	s_mov_b32 s50, s35
	v_readlane_b32 s9, v251, 10
	s_add_u32 s8, s70, 0x4bc00000
	s_addc_u32 s9, s71, 0
	s_cmp_eq_u32 s4, 0
	s_cselect_b32 s51, s5, s2
	s_cmpk_gt_i32 s51, 0x1ff
	s_waitcnt lgkmcnt(0)
	s_barrier
	s_cbranch_scc1 .LBB0_1053
	s_add_u32 s4, s70, 0x3da00000
	s_addc_u32 s5, s71, 0
	s_add_u32 s10, s70, 0x3c200000
	s_addc_u32 s11, s71, 0
	s_movk_i32 s52, 0x2000
	s_mov_b32 s53, 0xc3e00000
	v_mov_b32_e32 v203, 0x43e00000
	v_mov_b32_e32 v191, 0
	s_movk_i32 s54, 0xd0
	s_movk_i32 s55, 0x3000
	s_mov_b32 s56, 0x5010400
	s_mov_b32 s57, 0x7030602
	s_mov_b32 s58, 0x5040100
	s_mov_b32 s59, 0x7060302
	s_add_i32 s60, 0, 0x6800
	s_movk_i32 s61, 0x1c00
	s_movk_i32 s62, 0x4000
	s_movk_i32 s63, 0x6000
	s_mov_b32 s64, 0x8000
	s_mov_b32 s65, 0xa000
	s_mov_b32 s66, 0xc000
	s_mov_b32 s67, 0xe000
	v_mov_b32_e32 v208, 0x1c00
	v_mov_b32_e32 v209, 0xff800000
	v_readlane_b32 s18, v251, 0
	v_readlane_b32 s19, v251, 1
	v_readlane_b32 s98, v251, 9
	s_nop 3
	s_sub_u32 s18, s18, 0x38
	s_subb_u32 s19, s19, 0
	s_load_dwordx4 s[44:47], s[18:19], 0x0
	s_mul_i32 s98, s98, 56
	s_add_i32 s99, s98, 56
	s_mov_b32 s100, 0
	s_waitcnt lgkmcnt(0)
	v_writelane_b32 v252, s44, 0
	v_writelane_b32 v252, s45, 1
	v_writelane_b32 v252, s46, 2
	v_writelane_b32 v252, s47, 3
	s_branch .LBB0_1023

;     __device__ __forceinline__ bool next(int i, Unit& u) const { if (!T.tile(i, u.pm, u.pn)) return false; u.aoff = (size_t)u.pm * atile; u.boff = (size_t)u.pn * btile; return true; }
;     __device__ __forceinline__ bool next(int i, Unit& u) const { if (!T.tile(i, u.pm, u.pn)) return false; u.aoff = (size_t)u.pm * 256 * D * 2 + (size_t)(u.pn >> 1) * 512; u.boff = (size_t)u.pn * 256 * 256 * 2; return true; }
;     __device__ __forceinline__ bool next(int i, Unit& u) const { if (!T.tile(i, u.pm, u.pn)) return false; const int e = tile_e[u.pm] & 7; u.aoff = (size_t)u.pm * atile; u.boff = ((size_t)e * nN + u.pn) * btile; return true; }
; #define PV_MMA() do { DSW4(4, va0, va1, va2, va3); o[0] = MMA8(CAT8(va0, va1), pf, o[0]); o[1] = MMA8(CAT8(va2, va3), pf, o[1]); \
;         DSW4(0, va4, va5, va6, va7); o[2] = MMA8(CAT8(va4, va5), pf, o[2]); o[3] = MMA8(CAT8(va6, va7), pf, o[3]); } while (0)
; __device__ __forceinline__ void attn_unit(LAS unsigned char* lds, const unsigned char* Q, const unsigned char* KV, const bf16_t* KPE, const float* CST, bf16_t* O, int b, int h, int qb, CvtState& cs) {
;     ...
;     for (int t = 0; t < NT; ++t) {
;         if (t + 1 < NT) ATT_LOAD(t + 1);
;         if (cvt_pend) { cvt_store(cs, lane, cv); cvt_pend = false; }
;         if (lag && pend) { PV_MMA(); pend = false; }
;         const int kb0 = t * 64;
;         const bool cvt_now = ((t & 3) == 0) && cs.next < cs.end;
;         if (cvt_now && !(kb0 <= qlo + 31)) cvt_load(cs, lane, cv);
; template <int MODE>
; __device__ __forceinline__ void tr_matrix6(const float* W, int nb, int K, int N, unsigned char* WT, int drows, int rot, int gw, int NGW, int lane, float wscale) {
;     ...
;         const int e = it / per, r = it - e * per, kb = r / nbn, nbk = r - kb * nbn, n0 = nbk * 32, k0 = kb * 256;
;         const float* src = W + (size_t)e * K * N + (size_t)(k0 + 32 * q) * N + n0 + 4 * c;
;         f32x4 v[32];
; #pragma unroll
;         for (int i = 0; i < 32; ++i) v[i] = *(const f32x4*)(src + (size_t)i * N);
.LBB0_1037:
	s_and_b32 s18, s89, 3
	s_cmp_eq_u32 s18, 1
	s_cbranch_scc0 .Lf6_noload_a
	s_cmp_lt_i32 s98, s99
	s_cbranch_scc0 .Lf6_noload_a
	s_mul_hi_u32 s18, s98, 0x2492493
	s_mul_i32 s19, s18, 0x70
	s_sub_u32 s19, s98, s19
	s_and_b32 s20, s18, 63
	s_lshr_b32 s18, s18, 6
	s_and_b32 s21, s18, 7
	s_lshr_b32 s18, s18, 3
	s_lshl_b32 s21, s21, 11
	s_lshl_b32 s20, s20, 5
	s_add_u32 s21, s21, s20
	s_mul_i32 s21, s21, 0x7000
	s_lshl_b32 s19, s19, 8
	s_add_u32 s21, s21, s19
	s_lshl_b32 s20, s18, 1
	s_nop 3
	v_readlane_b32 s18, v252, s20
	s_add_u32 s20, s20, 1
	s_nop 3
	v_readlane_b32 s19, v252, s20
	s_nop 3
	s_add_u32 s18, s18, s21
	s_addc_u32 s19, s19, 0
	v_mbcnt_lo_u32_b32 v218, -1, 0
	v_mbcnt_hi_u32_b32 v218, -1, v218
	v_lshlrev_b32_e32 v218, 2, v218
	global_load_dword v158, v218, s[18:19]
	s_add_u32 s18, s18, 0x7000
	s_addc_u32 s19, s19, 0
	global_load_dword v159, v218, s[18:19]
	s_add_u32 s18, s18, 0x7000
	s_addc_u32 s19, s19, 0
	global_load_dword v160, v218, s[18:19]
	s_add_u32 s18, s18, 0x7000
	s_addc_u32 s19, s19, 0
	global_load_dword v161, v218, s[18:19]
	s_add_u32 s18, s18, 0x7000
	s_addc_u32 s19, s19, 0
	global_load_dword v162, v218, s[18:19]
	s_add_u32 s18, s18, 0x7000
	s_addc_u32 s19, s19, 0
	global_load_dword v163, v218, s[18:19]
	s_add_u32 s18, s18, 0x7000
	s_addc_u32 s19, s19, 0
	global_load_dword v164, v218, s[18:19]
	s_add_u32 s18, s18, 0x7000
	s_addc_u32 s19, s19, 0
	global_load_dword v165, v218, s[18:19]
	s_add_u32 s18, s18, 0x7000
	s_addc_u32 s19, s19, 0
	global_load_dword v166, v218, s[18:19]
	s_add_u32 s18, s18, 0x7000
	s_addc_u32 s19, s19, 0
	global_load_dword v167, v218, s[18:19]
	s_add_u32 s18, s18, 0x7000
	s_addc_u32 s19, s19, 0
	global_load_dword v168, v218, s[18:19]
	s_add_u32 s18, s18, 0x7000
	s_addc_u32 s19, s19, 0
	global_load_dword v169, v218, s[18:19]
	s_add_u32 s18, s18, 0x7000
	s_addc_u32 s19, s19, 0
	global_load_dword v170, v218, s[18:19]
	s_add_u32 s18, s18, 0x7000
	s_addc_u32 s19, s19, 0
	global_load_dword v171, v218, s[18:19]
	s_add_u32 s18, s18, 0x7000
	s_addc_u32 s19, s19, 0
	global_load_dword v172, v218, s[18:19]
	s_add_u32 s18, s18, 0x7000
	s_addc_u32 s19, s19, 0
	global_load_dword v173, v218, s[18:19]
	s_add_u32 s18, s18, 0x7000
	s_addc_u32 s19, s19, 0
	global_load_dword v174, v218, s[18:19]
	s_add_u32 s18, s18, 0x7000
	s_addc_u32 s19, s19, 0
	global_load_dword v175, v218, s[18:19]
	s_add_u32 s18, s18, 0x7000
	s_addc_u32 s19, s19, 0
	global_load_dword v176, v218, s[18:19]
	s_add_u32 s18, s18, 0x7000
	s_addc_u32 s19, s19, 0
	global_load_dword v177, v218, s[18:19]
	s_add_u32 s18, s18, 0x7000
	s_addc_u32 s19, s19, 0
	global_load_dword v178, v218, s[18:19]
	s_add_u32 s18, s18, 0x7000
	s_addc_u32 s19, s19, 0
	global_load_dword v179, v218, s[18:19]
	s_add_u32 s18, s18, 0x7000
	s_addc_u32 s19, s19, 0
	global_load_dword v180, v218, s[18:19]
	s_add_u32 s18, s18, 0x7000
	s_addc_u32 s19, s19, 0
	global_load_dword v181, v218, s[18:19]
	s_add_u32 s18, s18, 0x7000
	s_addc_u32 s19, s19, 0
	global_load_dword v182, v218, s[18:19]
	s_add_u32 s18, s18, 0x7000
	s_addc_u32 s19, s19, 0
	global_load_dword v183, v218, s[18:19]
	s_add_u32 s18, s18, 0x7000
	s_addc_u32 s19, s19, 0
	global_load_dword v184, v218, s[18:19]
	s_add_u32 s18, s18, 0x7000
	s_addc_u32 s19, s19, 0
	global_load_dword v185, v218, s[18:19]
	s_add_u32 s18, s18, 0x7000
	s_addc_u32 s19, s19, 0
	global_load_dword v186, v218, s[18:19]
	s_add_u32 s18, s18, 0x7000
	s_addc_u32 s19, s19, 0
	global_load_dword v187, v218, s[18:19]
	s_add_u32 s18, s18, 0x7000
	s_addc_u32 s19, s19, 0
	global_load_dword v188, v218, s[18:19]
	s_add_u32 s18, s18, 0x7000
	s_addc_u32 s19, s19, 0
	global_load_dword v189, v218, s[18:19]
	s_mov_b32 s100, 1

; template <int MODE>
; __device__ __forceinline__ void tr_matrix6(const float* W, int nb, int K, int N, unsigned char* WT, int drows, int rot, int gw, int NGW, int lane, float wscale) {
;     ...
;         for (int j = 0; j < 4; ++j) { float x[32];
; #pragma unroll
;             for (int i = 0; i < 32; ++i) x[i] = v[i][j] * wscale;
;             const v6u w = pk32_fp6(x);
;             *(u32x4*)(dst + (size_t)j * K) = (u32x4){w[0], w[1], w[2], w[3]}; *(u32x4*)(dst + (size_t)j * K + 16) = (u32x4){w[4], w[5], 0u, 0u}; }
.LBB0_1047:
	s_cmp_lg_u32 s100, 0
	s_cbranch_scc0 .Lf6_nostore
	s_and_b32 s18, s89, 2
	s_cmp_eq_u32 s18, 2
	s_cbranch_scc0 .Lf6_nostore
	s_mul_hi_u32 s18, s98, 0x2492493
	s_mul_i32 s19, s18, 0x70
	s_sub_u32 s19, s98, s19
	s_and_b32 s20, s18, 63
	s_lshr_b32 s18, s18, 6
	s_and_b32 s21, s18, 7
	s_lshr_b32 s18, s18, 3
	s_lshr_b32 s101, s19, 1
	s_lshl_b32 s101, s101, 8
	s_and_b32 s19, s19, 1
	s_lshl_b32 s19, s19, 6
	s_add_u32 s19, s19, s101
	s_lshl_b32 s18, s18, 7
	s_add_u32 s19, s19, s18
	s_mul_i32 s21, s21, 0x3800
	s_add_u32 s19, s19, s21
	s_lshl_b32 s19, s19, 11
	s_lshl_b32 s20, s20, 5
	s_add_u32 s19, s19, s20
	s_add_u32 s19, s19, 0x8a00000
	s_add_u32 s20, s70, s19
	s_addc_u32 s21, s71, 0
	v_mbcnt_lo_u32_b32 v218, -1, 0
	v_mbcnt_hi_u32_b32 v218, -1, v218
	v_lshlrev_b32_e32 v218, 11, v218
	v_mov_b32_e32 v219, 0x40f00000
	s_mov_b32 s18, 0xc0f00000
	v_mov_b32_e32 v80, 0
	v_mov_b32_e32 v81, 0
	s_waitcnt vmcnt(0)
	v_mul_f32_e32 v158, 0x42b40000, v158
	v_mul_f32_e32 v159, 0x42b40000, v159
	v_mul_f32_e32 v160, 0x42b40000, v160
	v_mul_f32_e32 v161, 0x42b40000, v161
	v_mul_f32_e32 v162, 0x42b40000, v162
	v_mul_f32_e32 v163, 0x42b40000, v163
	v_mul_f32_e32 v164, 0x42b40000, v164
	v_mul_f32_e32 v165, 0x42b40000, v165
	v_mul_f32_e32 v166, 0x42b40000, v166
	v_mul_f32_e32 v167, 0x42b40000, v167
	v_mul_f32_e32 v168, 0x42b40000, v168
	v_mul_f32_e32 v169, 0x42b40000, v169
	v_mul_f32_e32 v170, 0x42b40000, v170
	v_mul_f32_e32 v171, 0x42b40000, v171
	v_mul_f32_e32 v172, 0x42b40000, v172
	v_mul_f32_e32 v173, 0x42b40000, v173
	v_mul_f32_e32 v174, 0x42b40000, v174
	v_mul_f32_e32 v175, 0x42b40000, v175
	v_mul_f32_e32 v176, 0x42b40000, v176
	v_mul_f32_e32 v177, 0x42b40000, v177
	v_mul_f32_e32 v178, 0x42b40000, v178
	v_mul_f32_e32 v179, 0x42b40000, v179
	v_mul_f32_e32 v180, 0x42b40000, v180
	v_mul_f32_e32 v181, 0x42b40000, v181
	v_mul_f32_e32 v182, 0x42b40000, v182
	v_mul_f32_e32 v183, 0x42b40000, v183
	v_mul_f32_e32 v184, 0x42b40000, v184
	v_mul_f32_e32 v185, 0x42b40000, v185
	v_mul_f32_e32 v186, 0x42b40000, v186
	v_mul_f32_e32 v187, 0x42b40000, v187
	v_mul_f32_e32 v188, 0x42b40000, v188
	v_mul_f32_e32 v189, 0x42b40000, v189
	v_med3_f32 v158, v158, s18, v219
	v_med3_f32 v159, v159, s18, v219
	v_med3_f32 v160, v160, s18, v219
	v_med3_f32 v161, v161, s18, v219
	v_med3_f32 v162, v162, s18, v219
	v_med3_f32 v163, v163, s18, v219
	v_med3_f32 v164, v164, s18, v219
	v_med3_f32 v165, v165, s18, v219
	v_med3_f32 v166, v166, s18, v219
	v_med3_f32 v167, v167, s18, v219
	v_med3_f32 v168, v168, s18, v219
	v_med3_f32 v169, v169, s18, v219
	v_med3_f32 v170, v170, s18, v219
	v_med3_f32 v171, v171, s18, v219
	v_med3_f32 v172, v172, s18, v219
	v_med3_f32 v173, v173, s18, v219
	v_med3_f32 v174, v174, s18, v219
	v_med3_f32 v175, v175, s18, v219
	v_med3_f32 v176, v176, s18, v219
	v_med3_f32 v177, v177, s18, v219
	v_med3_f32 v178, v178, s18, v219
	v_med3_f32 v179, v179, s18, v219
	v_med3_f32 v180, v180, s18, v219
	v_med3_f32 v181, v181, s18, v219
	v_med3_f32 v182, v182, s18, v219
	v_med3_f32 v183, v183, s18, v219
	v_med3_f32 v184, v184, s18, v219
	v_med3_f32 v185, v185, s18, v219
	v_med3_f32 v186, v186, s18, v219
	v_med3_f32 v187, v187, s18, v219
	v_med3_f32 v188, v188, s18, v219
	v_med3_f32 v189, v189, s18, v219
	v_cvt_scalef32_2xpk16_fp6_f32 v[74:79], v[158:173], v[174:189], 1.0
	s_nop 1
	global_store_dwordx4 v218, v[74:77], s[20:21]
	global_store_dwordx4 v218, v[78:81], s[20:21] offset:16
	s_add_i32 s98, s98, 1
	s_mov_b32 s100, 0

;     __device__ __forceinline__ bool next(int i, Unit& u) const { if (!T.tile(i, u.pm, u.pn)) return false; u.aoff = (size_t)u.pm * atile; u.boff = (size_t)u.pn * btile; return true; }
;     __device__ __forceinline__ bool next(int i, Unit& u) const { if (!T.tile(i, u.pm, u.pn)) return false; u.aoff = (size_t)u.pm * 256 * D * 2 + (size_t)(u.pn >> 1) * 512; u.boff = (size_t)u.pn * 256 * 256 * 2; return true; }
;     __device__ __forceinline__ bool next(int i, Unit& u) const { if (!T.tile(i, u.pm, u.pn)) return false; const int e = tile_e[u.pm] & 7; u.aoff = (size_t)u.pm * atile; u.boff = ((size_t)e * nN + u.pn) * btile; return true; }
; #define PV_MMA() do { DSW4(4, va0, va1, va2, va3); o[0] = MMA8(CAT8(va0, va1), pf, o[0]); o[1] = MMA8(CAT8(va2, va3), pf, o[1]); \
;         DSW4(0, va4, va5, va6, va7); o[2] = MMA8(CAT8(va4, va5), pf, o[2]); o[3] = MMA8(CAT8(va6, va7), pf, o[3]); } while (0)
; __device__ __forceinline__ void attn_unit(LAS unsigned char* lds, const unsigned char* Q, const unsigned char* KV, const bf16_t* KPE, const float* CST, bf16_t* O, int b, int h, int qb, CvtState& cs) {
;     ...
;     for (int t = 0; t < NT; ++t) {
;         if (t + 1 < NT) ATT_LOAD(t + 1);
;         if (cvt_pend) { cvt_store(cs, lane, cv); cvt_pend = false; }
;         if (lag && pend) { PV_MMA(); pend = false; }
;         const int kb0 = t * 64;
;         const bool cvt_now = ((t & 3) == 0) && cs.next < cs.end;
;         if (cvt_now && !(kb0 <= qlo + 31)) cvt_load(cs, lane, cv);
; template <int MODE>
; __device__ __forceinline__ void tr_matrix6(const float* W, int nb, int K, int N, unsigned char* WT, int drows, int rot, int gw, int NGW, int lane, float wscale) {
;     ...
;         const int e = it / per, r = it - e * per, kb = r / nbn, nbk = r - kb * nbn, n0 = nbk * 32, k0 = kb * 256;
;         const float* src = W + (size_t)e * K * N + (size_t)(k0 + 32 * q) * N + n0 + 4 * c;
;         f32x4 v[32];
; #pragma unroll
;         for (int i = 0; i < 32; ++i) v[i] = *(const f32x4*)(src + (size_t)i * N);
.LBB0_1049:
	s_add_u32 s18, s89, 3
	s_and_b32 s18, s18, 3
	s_cmp_lt_u32 s18, 2
	s_cbranch_scc0 .Lf6_noload_b
	s_cmp_lt_i32 s98, s99
	s_cbranch_scc0 .Lf6_noload_b
	s_cmp_lg_u32 s100, 0
	s_cbranch_scc1 .Lf6_noload_b
	s_mul_hi_u32 s18, s98, 0x2492493
	s_mul_i32 s19, s18, 0x70
	s_sub_u32 s19, s98, s19
	s_and_b32 s20, s18, 63
	s_lshr_b32 s18, s18, 6
	s_and_b32 s21, s18, 7
	s_lshr_b32 s18, s18, 3
	s_lshl_b32 s21, s21, 11
	s_lshl_b32 s20, s20, 5
	s_add_u32 s21, s21, s20
	s_mul_i32 s21, s21, 0x7000
	s_lshl_b32 s19, s19, 8
	s_add_u32 s21, s21, s19
	s_lshl_b32 s20, s18, 1
	s_nop 3
	v_readlane_b32 s18, v252, s20
	s_add_u32 s20, s20, 1
	s_nop 3
	v_readlane_b32 s19, v252, s20
	s_nop 3
	s_add_u32 s18, s18, s21
	s_addc_u32 s19, s19, 0
	v_mbcnt_lo_u32_b32 v218, -1, 0
	v_mbcnt_hi_u32_b32 v218, -1, v218
	v_lshlrev_b32_e32 v218, 2, v218
	global_load_dword v158, v218, s[18:19]
	s_add_u32 s18, s18, 0x7000
	s_addc_u32 s19, s19, 0
	global_load_dword v159, v218, s[18:19]
	s_add_u32 s18, s18, 0x7000
	s_addc_u32 s19, s19, 0
	global_load_dword v160, v218, s[18:19]
	s_add_u32 s18, s18, 0x7000
	s_addc_u32 s19, s19, 0
	global_load_dword v161, v218, s[18:19]
	s_add_u32 s18, s18, 0x7000
	s_addc_u32 s19, s19, 0
	global_load_dword v162, v218, s[18:19]
	s_add_u32 s18, s18, 0x7000
	s_addc_u32 s19, s19, 0
	global_load_dword v163, v218, s[18:19]
	s_add_u32 s18, s18, 0x7000
	s_addc_u32 s19, s19, 0
	global_load_dword v164, v218, s[18:19]
	s_add_u32 s18, s18, 0x7000
	s_addc_u32 s19, s19, 0
	global_load_dword v165, v218, s[18:19]
	s_add_u32 s18, s18, 0x7000
	s_addc_u32 s19, s19, 0
	global_load_dword v166, v218, s[18:19]
	s_add_u32 s18, s18, 0x7000
	s_addc_u32 s19, s19, 0
	global_load_dword v167, v218, s[18:19]
	s_add_u32 s18, s18, 0x7000
	s_addc_u32 s19, s19, 0
	global_load_dword v168, v218, s[18:19]
	s_add_u32 s18, s18, 0x7000
	s_addc_u32 s19, s19, 0
	global_load_dword v169, v218, s[18:19]
	s_add_u32 s18, s18, 0x7000
	s_addc_u32 s19, s19, 0
	global_load_dword v170, v218, s[18:19]
	s_add_u32 s18, s18, 0x7000
	s_addc_u32 s19, s19, 0
	global_load_dword v171, v218, s[18:19]
	s_add_u32 s18, s18, 0x7000
	s_addc_u32 s19, s19, 0
	global_load_dword v172, v218, s[18:19]
	s_add_u32 s18, s18, 0x7000
	s_addc_u32 s19, s19, 0
	global_load_dword v173, v218, s[18:19]
	s_add_u32 s18, s18, 0x7000
	s_addc_u32 s19, s19, 0
	global_load_dword v174, v218, s[18:19]
	s_add_u32 s18, s18, 0x7000
	s_addc_u32 s19, s19, 0
	global_load_dword v175, v218, s[18:19]
	s_add_u32 s18, s18, 0x7000
	s_addc_u32 s19, s19, 0
	global_load_dword v176, v218, s[18:19]
	s_add_u32 s18, s18, 0x7000
	s_addc_u32 s19, s19, 0
	global_load_dword v177, v218, s[18:19]
	s_add_u32 s18, s18, 0x7000
	s_addc_u32 s19, s19, 0
	global_load_dword v178, v218, s[18:19]
	s_add_u32 s18, s18, 0x7000
	s_addc_u32 s19, s19, 0
	global_load_dword v179, v218, s[18:19]
	s_add_u32 s18, s18, 0x7000
	s_addc_u32 s19, s19, 0
	global_load_dword v180, v218, s[18:19]
	s_add_u32 s18, s18, 0x7000
	s_addc_u32 s19, s19, 0
	global_load_dword v181, v218, s[18:19]
	s_add_u32 s18, s18, 0x7000
	s_addc_u32 s19, s19, 0
	global_load_dword v182, v218, s[18:19]
	s_add_u32 s18, s18, 0x7000
	s_addc_u32 s19, s19, 0
	global_load_dword v183, v218, s[18:19]
	s_add_u32 s18, s18, 0x7000
	s_addc_u32 s19, s19, 0
	global_load_dword v184, v218, s[18:19]
	s_add_u32 s18, s18, 0x7000
	s_addc_u32 s19, s19, 0
	global_load_dword v185, v218, s[18:19]
	s_add_u32 s18, s18, 0x7000
	s_addc_u32 s19, s19, 0
	global_load_dword v186, v218, s[18:19]
	s_add_u32 s18, s18, 0x7000
	s_addc_u32 s19, s19, 0
	global_load_dword v187, v218, s[18:19]
	s_add_u32 s18, s18, 0x7000
	s_addc_u32 s19, s19, 0
	global_load_dword v188, v218, s[18:19]
	s_add_u32 s18, s18, 0x7000
	s_addc_u32 s19, s19, 0
	global_load_dword v189, v218, s[18:19]
	s_mov_b32 s100, 1
